# speedup vs baseline: 1.0009x; 1.0009x over previous
.LBB1_9:
	v_add_u32_e32 v182, s20, v209
	ds_read_b64_tr_b16 v[178:179], v182 offset:24576
	ds_read_b64_tr_b16 v[180:181], v182 offset:25088
	s_waitcnt lgkmcnt(9)
	v_mfma_f32_32x32x16_f16 v[98:113], v[174:177], v[142:145], v[34:49]
	s_mov_b64 s[2:3], 0
	v_add_f32_e32 v82, v66, v67
	v_add_f32_e32 v82, v68, v82
	v_add_f32_e32 v82, v69, v82
	v_add_f32_e32 v82, v70, v82
	v_add_f32_e32 v82, v71, v82
	v_cvt_pk_f16_f32 v134, v66, v67
	v_cvt_pk_f16_f32 v135, v68, v69
	ds_read_b64_tr_b16 v[174:175], v182 offset:28672
	ds_read_b64_tr_b16 v[176:177], v182 offset:29184
	v_add_f32_e32 v66, v72, v82
	s_waitcnt lgkmcnt(10)
	v_mfma_f32_32x32x16_f16 v[82:97], v[170:173], v[142:145], v[34:49]
	s_add_u32 s52, s16, 0xffffe000
	s_addc_u32 s53, s17, -1
	v_add_f32_e32 v66, v73, v66
	v_add_f32_e32 v66, v74, v66
	v_add_f32_e32 v66, v75, v66
	v_cvt_pk_f16_f32 v136, v70, v71
	v_cvt_pk_f16_f32 v137, v72, v73
	ds_read_b64_tr_b16 v[170:171], v182 offset:25600
	ds_read_b64_tr_b16 v[172:173], v182 offset:26112
	s_waitcnt lgkmcnt(11)
	v_mfma_f32_32x32x16_f16 v[98:113], v[166:169], v[138:141], v[98:113]
	v_add_f32_e32 v66, v76, v66
	v_add_f32_e32 v66, v77, v66
	v_add_f32_e32 v66, v78, v66
	v_add_f32_e32 v66, v79, v66
	v_cvt_pk_f16_f32 v126, v74, v75
	v_cvt_pk_f16_f32 v127, v76, v77
	ds_read_b64_tr_b16 v[74:75], v182 offset:29696
	ds_read_b64_tr_b16 v[76:77], v182 offset:30208
	s_waitcnt lgkmcnt(12)
	v_mfma_f32_32x32x16_f16 v[82:97], v[162:165], v[138:141], v[82:97]
	v_add_f32_e32 v66, v80, v66
	v_add_f32_e32 v66, v81, v66
	v_add_f32_e32 v66, v50, v66
	v_add_f32_e32 v66, v51, v66
	v_cvt_pk_f16_f32 v128, v78, v79
	v_cvt_pk_f16_f32 v129, v80, v81
	ds_read_b64_tr_b16 v[70:71], v182 offset:26624
	ds_read_b64_tr_b16 v[72:73], v182 offset:27136
	s_waitcnt lgkmcnt(13)
	v_mfma_f32_32x32x16_f16 v[98:113], v[158:161], v[130:133], v[98:113]
	v_add_f32_e32 v66, v52, v66
	v_add_f32_e32 v66, v53, v66
	v_add_f32_e32 v66, v54, v66
	v_add_f32_e32 v78, v55, v66
	v_cvt_pk_f16_f32 v118, v50, v51
	v_cvt_pk_f16_f32 v119, v52, v53
	ds_read_b64_tr_b16 v[66:67], v182 offset:30720
	ds_read_b64_tr_b16 v[68:69], v182 offset:31232
	s_waitcnt lgkmcnt(14)
	v_mfma_f32_32x32x16_f16 v[82:97], v[154:157], v[130:133], v[82:97]
	v_add_f32_e32 v50, v56, v78
	v_add_f32_e32 v50, v57, v50
	v_add_f32_e32 v50, v58, v50
	v_add_f32_e32 v50, v59, v50
	v_cvt_pk_f16_f32 v120, v54, v55
	v_cvt_pk_f16_f32 v121, v56, v57
	ds_read_b64_tr_b16 v[54:55], v182 offset:27648
	ds_read_b64_tr_b16 v[56:57], v182 offset:28160
	s_waitcnt lgkmcnt(14)
	v_mfma_f32_32x32x16_f16 v[98:113], v[150:153], v[122:125], v[98:113]
	v_add_f32_e32 v50, v60, v50
	v_add_f32_e32 v50, v61, v50
	v_add_f32_e32 v50, v62, v50
	v_add_f32_e32 v78, v63, v50
	v_cvt_pk_f16_f32 v114, v58, v59
	v_cvt_pk_f16_f32 v115, v60, v61
	ds_read_b64_tr_b16 v[50:51], v182 offset:31744
	ds_read_b64_tr_b16 v[52:53], v182 offset:32256
	v_mfma_f32_32x32x16_f16 v[82:97], v[146:149], v[122:125], v[82:97]
	v_add_f32_e32 v58, v64, v78
	v_add_f32_e32 v58, v65, v58
	v_cvt_pk_f16_f32 v116, v62, v63
	v_cvt_pk_f16_f32 v117, v64, v65
	v_max_f32_e32 v59, v98, v99
	v_max3_f32 v60, v100, v101, v102
	v_max3_f32 v59, v59, v103, v104
	v_max3_f32 v60, v60, v105, v106
	v_max3_f32 v59, v59, v107, v108
	v_max3_f32 v60, v60, v109, v110
	v_max3_f32 v59, v59, v111, v112
	v_add_f32_e32 v182, v203, v58
	v_max3_f32 v60, v60, v113, v82
	v_max3_f32 v59, v59, v83, v84
	v_max3_f32 v60, v60, v85, v86
	v_max3_f32 v59, v59, v87, v88
	v_max3_f32 v60, v60, v89, v90
	v_max3_f32 v59, v59, v91, v92
	v_max3_f32 v60, v60, v93, v94
	v_max3_f32 v59, v59, v95, v96
	v_max3_f32 v58, v59, v60, v97
	v_cmp_lt_f32_e32 vcc, s23, v58
	s_cmp_lg_u64 vcc, 0
	s_cbranch_scc1 .LBB1_17

.LBB1_12:
	s_add_i32 s2, s22, 0x2000
	s_cmpk_lg_i32 s22, 0x4000
	s_cselect_b32 s43, s2, 0
	v_add_u32_e32 v183, s24, v209
	ds_read_b64_tr_b16 v[154:155], v183 offset:24576
	ds_read_b64_tr_b16 v[156:157], v183 offset:25088
	s_waitcnt lgkmcnt(9)
	v_mfma_f32_32x32x16_f16 v[66:81], v[58:61], v[142:145], v[34:49]
	s_mov_b64 s[2:3], 0
	v_add_f32_e32 v50, v98, v99
	v_add_f32_e32 v50, v100, v50
	v_add_f32_e32 v50, v101, v50
	v_add_f32_e32 v50, v102, v50
	v_add_f32_e32 v50, v103, v50
	v_cvt_pk_f16_f32 v134, v98, v99
	v_cvt_pk_f16_f32 v135, v100, v101
	ds_read_b64_tr_b16 v[150:151], v183 offset:28672
	ds_read_b64_tr_b16 v[152:153], v183 offset:29184
	v_add_f32_e32 v50, v104, v50
	v_add_f32_e32 v50, v105, v50
	v_add_f32_e32 v50, v106, v50
	v_add_f32_e32 v98, v107, v50
	s_waitcnt lgkmcnt(10)
	v_mfma_f32_32x32x16_f16 v[50:65], v[146:149], v[142:145], v[34:49]
	s_add_u32 s52, s18, 0x2000
	s_addc_u32 s53, s19, 0
	v_cvt_pk_f16_f32 v136, v102, v103
	v_cvt_pk_f16_f32 v137, v104, v105
	ds_read_b64_tr_b16 v[146:147], v183 offset:25600
	ds_read_b64_tr_b16 v[148:149], v183 offset:26112
	s_waitcnt lgkmcnt(11)
	v_mfma_f32_32x32x16_f16 v[66:81], v[178:181], v[138:141], v[66:81]
	v_add_f32_e32 v98, v108, v98
	v_add_f32_e32 v98, v109, v98
	v_add_f32_e32 v98, v110, v98
	v_add_f32_e32 v98, v111, v98
	v_cvt_pk_f16_f32 v126, v106, v107
	v_cvt_pk_f16_f32 v127, v108, v109
	ds_read_b64_tr_b16 v[106:107], v183 offset:29696
	ds_read_b64_tr_b16 v[108:109], v183 offset:30208
	s_waitcnt lgkmcnt(12)
	v_mfma_f32_32x32x16_f16 v[50:65], v[170:173], v[138:141], v[50:65]
	v_add_f32_e32 v98, v112, v98
	v_add_f32_e32 v98, v113, v98
	v_add_f32_e32 v98, v82, v98
	v_add_f32_e32 v98, v83, v98
	v_cvt_pk_f16_f32 v128, v110, v111
	v_cvt_pk_f16_f32 v129, v112, v113
	ds_read_b64_tr_b16 v[102:103], v183 offset:26624
	ds_read_b64_tr_b16 v[104:105], v183 offset:27136
	s_waitcnt lgkmcnt(13)
	v_mfma_f32_32x32x16_f16 v[66:81], v[174:177], v[130:133], v[66:81]
	v_add_f32_e32 v98, v84, v98
	v_add_f32_e32 v98, v85, v98
	v_add_f32_e32 v98, v86, v98
	v_add_f32_e32 v110, v87, v98
	v_cvt_pk_f16_f32 v118, v82, v83
	v_cvt_pk_f16_f32 v119, v84, v85
	ds_read_b64_tr_b16 v[98:99], v183 offset:30720
	ds_read_b64_tr_b16 v[100:101], v183 offset:31232
	s_waitcnt lgkmcnt(14)
	v_mfma_f32_32x32x16_f16 v[50:65], v[162:165], v[130:133], v[50:65]
	v_add_f32_e32 v82, v88, v110
	v_add_f32_e32 v82, v89, v82
	v_add_f32_e32 v82, v90, v82
	v_add_f32_e32 v82, v91, v82
	v_cvt_pk_f16_f32 v120, v86, v87
	v_cvt_pk_f16_f32 v121, v88, v89
	ds_read_b64_tr_b16 v[86:87], v183 offset:27648
	ds_read_b64_tr_b16 v[88:89], v183 offset:28160
	s_waitcnt lgkmcnt(14)
	v_mfma_f32_32x32x16_f16 v[66:81], v[166:169], v[122:125], v[66:81]
	v_add_f32_e32 v82, v92, v82
	v_add_f32_e32 v82, v93, v82
	v_add_f32_e32 v82, v94, v82
	v_add_f32_e32 v110, v95, v82
	v_cvt_pk_f16_f32 v114, v90, v91
	v_cvt_pk_f16_f32 v115, v92, v93
	ds_read_b64_tr_b16 v[82:83], v183 offset:31744
	ds_read_b64_tr_b16 v[84:85], v183 offset:32256
	v_mfma_f32_32x32x16_f16 v[50:65], v[158:161], v[122:125], v[50:65]
	v_add_f32_e32 v90, v96, v110
	v_add_f32_e32 v90, v97, v90
	v_cvt_pk_f16_f32 v116, v94, v95
	v_cvt_pk_f16_f32 v117, v96, v97
	v_max_f32_e32 v91, v66, v67
	v_max3_f32 v92, v68, v69, v70
	v_max3_f32 v91, v91, v71, v72
	v_max3_f32 v92, v92, v73, v74
	v_max3_f32 v91, v91, v75, v76
	v_max3_f32 v92, v92, v77, v78
	v_max3_f32 v91, v91, v79, v80
	v_add_f32_e32 v203, v182, v90
	v_max3_f32 v92, v92, v81, v50
	v_max3_f32 v91, v91, v51, v52
	v_max3_f32 v92, v92, v53, v54
	v_max3_f32 v91, v91, v55, v56
	v_max3_f32 v92, v92, v57, v58
	v_max3_f32 v91, v91, v59, v60
	v_max3_f32 v92, v92, v61, v62
	v_max3_f32 v91, v91, v63, v64
	v_max3_f32 v90, v91, v92, v65
	v_cmp_lt_f32_e32 vcc, s23, v90
	s_cmp_lg_u64 vcc, 0
	s_cbranch_scc1 .LBB1_20

.LBB1_87:
	v_add_u32_e32 v65, s6, v251
	ds_read_b64_tr_b16 v[192:193], v65
	ds_read_b64_tr_b16 v[194:195], v65 offset:512
	s_waitcnt lgkmcnt(9)
	v_mfma_f32_32x32x16_f16 v[112:127], v[188:191], v[140:143], v[32:47]
	s_mov_b64 s[6:7], 0
	v_add_f32_e32 v66, v80, v81
	v_add_f32_e32 v66, v82, v66
	v_add_f32_e32 v66, v83, v66
	v_add_f32_e32 v66, v84, v66
	v_add_f32_e32 v66, v85, v66
	v_cvt_pk_f16_f32 v156, v80, v81
	v_cvt_pk_f16_f32 v157, v82, v83
	ds_read_b64_tr_b16 v[188:189], v65 offset:4096
	ds_read_b64_tr_b16 v[190:191], v65 offset:4608
	s_waitcnt lgkmcnt(10)
	v_mfma_f32_32x32x16_f16 v[96:111], v[184:187], v[140:143], v[32:47]
	s_add_u32 s52, s4, 0xffffe000
	s_addc_u32 s53, s5, -1
	v_add_f32_e32 v66, v86, v66
	v_add_f32_e32 v66, v87, v66
	v_add_f32_e32 v66, v88, v66
	v_add_f32_e32 v66, v89, v66
	v_cvt_pk_f16_f32 v158, v84, v85
	v_cvt_pk_f16_f32 v159, v86, v87
	ds_read_b64_tr_b16 v[78:79], v65 offset:1024
	ds_read_b64_tr_b16 v[80:81], v65 offset:1536
	s_waitcnt lgkmcnt(11)
	v_mfma_f32_32x32x16_f16 v[112:127], v[180:183], v[136:139], v[112:127]
	v_add_f32_e32 v66, v90, v66
	v_add_f32_e32 v66, v91, v66
	v_add_f32_e32 v66, v92, v66
	v_add_f32_e32 v66, v93, v66
	v_cvt_pk_f16_f32 v152, v88, v89
	v_cvt_pk_f16_f32 v153, v90, v91
	ds_read_b64_tr_b16 v[74:75], v65 offset:5120
	ds_read_b64_tr_b16 v[76:77], v65 offset:5632
	s_waitcnt lgkmcnt(12)
	v_mfma_f32_32x32x16_f16 v[96:111], v[176:179], v[136:139], v[96:111]
	v_add_f32_e32 v66, v94, v66
	v_add_f32_e32 v66, v95, v66
	v_add_f32_e32 v66, v48, v66
	v_add_f32_e32 v66, v49, v66
	v_cvt_pk_f16_f32 v154, v92, v93
	v_cvt_pk_f16_f32 v155, v94, v95
	ds_read_b64_tr_b16 v[70:71], v65 offset:2048
	ds_read_b64_tr_b16 v[72:73], v65 offset:2560
	s_waitcnt lgkmcnt(13)
	v_mfma_f32_32x32x16_f16 v[112:127], v[172:175], v[132:135], v[112:127]
	v_add_f32_e32 v66, v50, v66
	v_add_f32_e32 v66, v51, v66
	v_add_f32_e32 v66, v52, v66
	v_add_f32_e32 v82, v53, v66
	v_cvt_pk_f16_f32 v148, v48, v49
	v_cvt_pk_f16_f32 v149, v50, v51
	ds_read_b64_tr_b16 v[66:67], v65 offset:6144
	ds_read_b64_tr_b16 v[68:69], v65 offset:6656
	s_waitcnt lgkmcnt(14)
	v_mfma_f32_32x32x16_f16 v[96:111], v[168:171], v[132:135], v[96:111]
	v_add_f32_e32 v48, v54, v82
	v_add_f32_e32 v48, v55, v48
	v_add_f32_e32 v48, v56, v48
	v_add_f32_e32 v48, v57, v48
	v_cvt_pk_f16_f32 v150, v52, v53
	v_cvt_pk_f16_f32 v151, v54, v55
	ds_read_b64_tr_b16 v[52:53], v65 offset:3072
	ds_read_b64_tr_b16 v[54:55], v65 offset:3584
	s_waitcnt lgkmcnt(14)
	v_mfma_f32_32x32x16_f16 v[112:127], v[164:167], v[128:131], v[112:127]
	v_add_f32_e32 v48, v58, v48
	v_add_f32_e32 v48, v59, v48
	v_add_f32_e32 v48, v60, v48
	v_add_f32_e32 v82, v61, v48
	v_cvt_pk_f16_f32 v144, v56, v57
	v_cvt_pk_f16_f32 v145, v58, v59
	ds_read_b64_tr_b16 v[48:49], v65 offset:7168
	ds_read_b64_tr_b16 v[50:51], v65 offset:7680
	v_mfma_f32_32x32x16_f16 v[96:111], v[160:163], v[128:131], v[96:111]
	v_add_f32_e32 v56, v62, v82
	v_add_f32_e32 v56, v63, v56
	v_cvt_pk_f16_f32 v146, v60, v61
	v_cvt_pk_f16_f32 v147, v62, v63
	v_max_f32_e32 v57, v112, v113
	v_max3_f32 v58, v114, v115, v116
	v_max3_f32 v57, v57, v117, v118
	v_max3_f32 v58, v58, v119, v120
	v_max3_f32 v57, v57, v121, v122
	v_max3_f32 v58, v58, v123, v124
	v_max3_f32 v57, v57, v125, v126
	v_add_f32_e32 v64, v64, v56
	v_max3_f32 v58, v58, v127, v96
	v_max3_f32 v57, v57, v97, v98
	v_max3_f32 v58, v58, v99, v100
	v_max3_f32 v57, v57, v101, v102
	v_max3_f32 v58, v58, v103, v104
	v_max3_f32 v57, v57, v105, v106
	v_max3_f32 v58, v58, v107, v108
	v_max3_f32 v57, v57, v109, v110
	v_max3_f32 v56, v57, v58, v111
	v_cmp_lt_f32_e32 vcc, s17, v56
	s_cmp_lg_u64 vcc, 0
	s_cbranch_scc1 .LBB1_95

.LBB1_90:
	s_add_i32 s6, s12, 0x2000
	s_cmpk_lg_i32 s12, 0x4000
	s_cselect_b32 s25, s6, 0
	v_add_u32_e32 v65, s30, v251
	ds_read_b64_tr_b16 v[168:169], v65
	ds_read_b64_tr_b16 v[170:171], v65 offset:512
	s_waitcnt lgkmcnt(9)
	v_mfma_f32_32x32x16_f16 v[80:95], v[56:59], v[140:143], v[32:47]
	s_mov_b64 s[6:7], 0
	v_add_f32_e32 v48, v112, v113
	v_add_f32_e32 v48, v114, v48
	v_add_f32_e32 v48, v115, v48
	v_add_f32_e32 v48, v116, v48
	v_add_f32_e32 v48, v117, v48
	v_cvt_pk_f16_f32 v156, v112, v113
	v_cvt_pk_f16_f32 v157, v114, v115
	ds_read_b64_tr_b16 v[164:165], v65 offset:4096
	ds_read_b64_tr_b16 v[166:167], v65 offset:4608
	v_add_f32_e32 v48, v118, v48
	v_add_f32_e32 v48, v119, v48
	v_add_f32_e32 v48, v120, v48
	v_add_f32_e32 v66, v121, v48
	s_waitcnt lgkmcnt(10)
	v_mfma_f32_32x32x16_f16 v[48:63], v[160:163], v[140:143], v[32:47]
	s_add_i32 s54, s12, s22
	s_add_i32 s55, s25, s23
	v_cvt_pk_f16_f32 v158, v116, v117
	v_cvt_pk_f16_f32 v159, v118, v119
	ds_read_b64_tr_b16 v[160:161], v65 offset:1024
	ds_read_b64_tr_b16 v[162:163], v65 offset:1536
	s_waitcnt lgkmcnt(11)
	v_mfma_f32_32x32x16_f16 v[80:95], v[188:191], v[136:139], v[80:95]
	v_add_f32_e32 v66, v122, v66
	v_add_f32_e32 v66, v123, v66
	v_add_f32_e32 v66, v124, v66
	v_add_f32_e32 v66, v125, v66
	v_cvt_pk_f16_f32 v152, v120, v121
	v_cvt_pk_f16_f32 v153, v122, v123
	ds_read_b64_tr_b16 v[116:117], v65 offset:5120
	ds_read_b64_tr_b16 v[118:119], v65 offset:5632
	s_waitcnt lgkmcnt(12)
	v_mfma_f32_32x32x16_f16 v[48:63], v[184:187], v[136:139], v[48:63]
	v_add_f32_e32 v66, v126, v66
	v_add_f32_e32 v66, v127, v66
	v_add_f32_e32 v66, v96, v66
	v_add_f32_e32 v66, v97, v66
	v_cvt_pk_f16_f32 v154, v124, v125
	v_cvt_pk_f16_f32 v155, v126, v127
	ds_read_b64_tr_b16 v[112:113], v65 offset:2048
	ds_read_b64_tr_b16 v[114:115], v65 offset:2560
	s_waitcnt lgkmcnt(13)
	v_mfma_f32_32x32x16_f16 v[80:95], v[74:77], v[132:135], v[80:95]
	v_add_f32_e32 v66, v98, v66
	v_add_f32_e32 v66, v99, v66
	v_add_f32_e32 v66, v100, v66
	v_add_f32_e32 v66, v101, v66
	v_cvt_pk_f16_f32 v148, v96, v97
	v_cvt_pk_f16_f32 v149, v98, v99
	ds_read_b64_tr_b16 v[74:75], v65 offset:6144
	ds_read_b64_tr_b16 v[76:77], v65 offset:6656
	s_waitcnt lgkmcnt(14)
	v_mfma_f32_32x32x16_f16 v[48:63], v[176:179], v[132:135], v[48:63]
	v_add_f32_e32 v66, v102, v66
	v_add_f32_e32 v66, v103, v66
	v_add_f32_e32 v66, v104, v66
	v_add_f32_e32 v66, v105, v66
	v_cvt_pk_f16_f32 v150, v100, v101
	v_cvt_pk_f16_f32 v151, v102, v103
	ds_read_b64_tr_b16 v[70:71], v65 offset:3072
	ds_read_b64_tr_b16 v[72:73], v65 offset:3584
	s_waitcnt lgkmcnt(14)
	v_mfma_f32_32x32x16_f16 v[80:95], v[180:183], v[128:131], v[80:95]
	v_add_f32_e32 v66, v106, v66
	v_add_f32_e32 v66, v107, v66
	v_add_f32_e32 v66, v108, v66
	v_add_f32_e32 v78, v109, v66
	v_cvt_pk_f16_f32 v144, v104, v105
	v_cvt_pk_f16_f32 v145, v106, v107
	ds_read_b64_tr_b16 v[66:67], v65 offset:7168
	ds_read_b64_tr_b16 v[68:69], v65 offset:7680
	v_mfma_f32_32x32x16_f16 v[48:63], v[172:175], v[128:131], v[48:63]
	v_add_f32_e32 v65, v110, v78
	v_add_f32_e32 v65, v111, v65
	v_cvt_pk_f16_f32 v146, v108, v109
	v_cvt_pk_f16_f32 v147, v110, v111
	v_max_f32_e32 v78, v80, v81
	v_max3_f32 v79, v82, v83, v84
	v_max3_f32 v78, v78, v85, v86
	v_max3_f32 v79, v79, v87, v88
	v_max3_f32 v78, v78, v89, v90
	v_max3_f32 v79, v79, v91, v92
	v_max3_f32 v78, v78, v93, v94
	v_add_f32_e32 v64, v64, v65
	v_max3_f32 v79, v79, v95, v48
	v_max3_f32 v78, v78, v49, v50
	v_max3_f32 v79, v79, v51, v52
	v_max3_f32 v78, v78, v53, v54
	v_max3_f32 v79, v79, v55, v56
	v_max3_f32 v78, v78, v57, v58
	v_max3_f32 v79, v79, v59, v60
	v_max3_f32 v78, v78, v61, v62
	v_max3_f32 v65, v78, v79, v63
	v_cmp_lt_f32_e32 vcc, s17, v65
	s_cmp_lg_u64 vcc, 0
	s_cbranch_scc1 .LBB1_98
